# MLA hot loop shifted by 4 bytes (one s_nop before its preheader, one after its exit): code-placement phase
# baseline (speedup 1.0000x reference)
.LBB0_557:
	v_lshlrev_b32_e32 v2, 4, v2
	s_lshl_b32 s33, s21, 10
	v_cndmask_b32_e64 v2, 0, v2, s[6:7]
	s_lshl_b32 s64, s20, 10
	s_ashr_i32 s49, s48, 31
	s_mul_i32 s7, s48, 0x1800
	v_lshlrev_b32_e32 v4, 4, v4
	s_mul_hi_i32 s6, s48, 0x1800
	s_add_u32 s7, s3, s7
	v_cndmask_b32_e64 v4, 0, v4, s[10:11]
	s_addc_u32 s10, s61, s6
	s_ashr_i32 s11, s87, 31
	s_add_u32 s6, s7, s87
	s_addc_u32 s7, s10, s11
	s_and_b32 s10, s19, 0x3fffffc0
	s_lshl_b32 s10, s10, 2
	s_add_i32 s51, s10, 0
	s_add_i32 s51, s51, 0x1e000
	s_lshl_b32 s65, s18, 10
	v_add_u32_e32 v211, v2, v3
	v_lshlrev_b32_e32 v2, 4, v6
	s_and_b64 s[10:11], s[52:53], exec
	v_cndmask_b32_e64 v2, 0, v2, s[14:15]
	s_cselect_b32 s11, s57, s59
	s_cselect_b32 s10, s56, s58
	s_mov_b32 s14, m0
	s_mov_b32 m0, s65
	s_nop 0
	global_load_lds_dwordx4 v211, s[10:11]
	s_mov_b32 m0, s14
	v_add_u32_e32 v210, v4, v5
	s_mov_b32 s10, m0
	s_mov_b32 m0, s64
	s_nop 0
	global_load_lds_dwordx4 v210, s[12:13]
	s_mov_b32 m0, s10
	v_add_u32_e32 v212, v2, v10
	s_mov_b32 s10, m0
	s_mov_b32 m0, s33
	s_nop 0
	global_load_lds_dwordx4 v212, s[12:13]
	s_mov_b32 m0, s10
	s_add_u32 s12, s56, 0x80000
	s_addc_u32 s13, s57, 0
	s_add_u32 s14, s58, 0x2000
	s_addc_u32 s15, s59, 0
	s_and_b64 s[10:11], s[52:53], exec
	s_cselect_b32 s11, s13, s15
	s_cselect_b32 s10, s12, s14
	s_add_i32 s16, s65, 0x5c00
	s_mov_b32 s17, m0
	s_mov_b32 m0, s16
	s_nop 0
	global_load_lds_dwordx4 v211, s[10:11]
	s_mov_b32 m0, s17
	s_and_b64 s[10:11], exec, s[54:55]
	v_and_b32_e32 v206, 31, v9
	s_cselect_b32 s11, s13, s15
	s_cselect_b32 s10, s12, s14
	s_lshl_b32 s50, s9, 5
	v_lshrrev_b32_e32 v207, 5, v8
	v_or_b32_e32 v4, s50, v206
	v_mov_b64_e32 v[2:3], s[6:7]
	s_movk_i32 s6, 0x1800
	s_add_i32 s12, s64, 0x5c00
	s_mov_b32 s13, m0
	s_mov_b32 m0, s12
	s_nop 0
	global_load_lds_dwordx4 v210, s[10:11]
	s_mov_b32 m0, s13
	v_mad_i64_i32 v[2:3], s[6:7], v4, s6, v[2:3]
	v_lshlrev_b32_e32 v204, 6, v207
	s_add_i32 s12, s33, 0x5c00
	s_mov_b32 s13, m0
	s_mov_b32 m0, s12
	s_nop 0
	global_load_lds_dwordx4 v212, s[10:11]
	s_mov_b32 m0, s13
	v_lshl_add_u64 v[2:3], v[2:3], 0, v[204:205]
	global_load_dwordx4 v[4:7], v[2:3], off
	global_load_dwordx4 v[10:13], v[2:3], off offset:16
	global_load_dwordx4 v[14:17], v[2:3], off offset:32
	global_load_dwordx4 v[18:21], v[2:3], off offset:48
	global_load_dwordx4 v[22:25], v[2:3], off offset:128
	global_load_dwordx4 v[26:29], v[2:3], off offset:144
	global_load_dwordx4 v[30:33], v[2:3], off offset:160
	global_load_dwordx4 v[34:37], v[2:3], off offset:176
	s_add_i32 s6, s50, s48
	v_and_b32_e32 v130, 32, v9
	v_add_u32_e32 v9, s6, v206
	v_lshlrev_b32_e32 v213, 2, v130
	v_cmp_gt_u32_e32 vcc, 32, v8
	s_add_u32 s9, s56, 0x100000
	s_addc_u32 s10, s57, 0
	s_add_u32 s11, s58, 0x4000
	s_addc_u32 s12, s59, 0
	s_and_b64 s[6:7], s[52:53], exec
	v_mad_u32_u24 v204, v206, s88, v130
	s_mov_b32 s22, s8
	s_mov_b32 s23, s8
	s_mov_b32 s15, s8
	s_mov_b32 s16, s8
	s_mov_b32 s17, s8
	s_mov_b32 s18, s8
	s_mov_b32 s19, s8
	s_mov_b32 s20, s8
	s_mov_b32 s21, s8
	s_waitcnt vmcnt(7)
	v_lshlrev_b32_e32 v183, 16, v4
	v_and_b32_e32 v181, 0xffff0000, v4
	v_lshlrev_b32_e32 v182, 16, v5
	v_and_b32_e32 v179, 0xffff0000, v5
	v_mov_b64_e32 v[4:5], s[42:43]
	s_waitcnt vmcnt(6)
	v_lshlrev_b32_e32 v176, 16, v10
	v_and_b32_e32 v173, 0xffff0000, v10
	v_lshlrev_b32_e32 v174, 16, v11
	v_and_b32_e32 v171, 0xffff0000, v11
	v_mad_i64_i32 v[10:11], s[6:7], v9, s89, v[4:5]
	v_lshlrev_b32_e32 v180, 16, v6
	v_and_b32_e32 v177, 0xffff0000, v6
	v_lshlrev_b32_e32 v178, 16, v7
	v_and_b32_e32 v175, 0xffff0000, v7
	v_lshlrev_b32_e32 v172, 16, v12
	v_and_b32_e32 v169, 0xffff0000, v12
	v_lshlrev_b32_e32 v170, 16, v13
	v_and_b32_e32 v167, 0xffff0000, v13
	s_waitcnt vmcnt(5)
	v_lshlrev_b32_e32 v168, 16, v14
	v_and_b32_e32 v165, 0xffff0000, v14
	v_lshlrev_b32_e32 v166, 16, v15
	v_and_b32_e32 v164, 0xffff0000, v15
	v_lshlrev_b32_e32 v163, 16, v16
	v_and_b32_e32 v161, 0xffff0000, v16
	v_lshlrev_b32_e32 v160, 16, v17
	v_and_b32_e32 v159, 0xffff0000, v17
	s_waitcnt vmcnt(4)
	v_lshlrev_b32_e32 v158, 16, v18
	v_and_b32_e32 v157, 0xffff0000, v18
	v_lshlrev_b32_e32 v156, 16, v19
	v_and_b32_e32 v155, 0xffff0000, v19
	v_lshlrev_b32_e32 v154, 16, v20
	v_and_b32_e32 v153, 0xffff0000, v20
	v_lshlrev_b32_e32 v152, 16, v21
	v_and_b32_e32 v151, 0xffff0000, v21
	global_load_dwordx4 v[4:7], v[10:11], off
	s_nop 0
	global_load_dwordx4 v[10:13], v[10:11], off offset:16
	s_nop 0
	global_load_dwordx4 v[64:67], v[2:3], off offset:288
	global_load_dwordx4 v[112:115], v[2:3], off offset:304
	global_load_dwordx4 v[76:79], v[2:3], off offset:256
	global_load_dwordx4 v[116:119], v[2:3], off offset:272
	global_load_dwordx4 v[120:123], v213, s[38:39] offset:608
	global_load_dwordx4 v[102:105], v213, s[38:39] offset:624
	global_load_dwordx4 v[14:17], v213, s[38:39] offset:560
	global_load_dwordx4 v[18:21], v213, s[38:39] offset:544
	v_mul_f32_e32 v202, v181, v181
	v_fmac_f32_e32 v202, v183, v183
	v_fmac_f32_e32 v202, v182, v182
	v_fmac_f32_e32 v202, v179, v179
	v_fmac_f32_e32 v202, v180, v180
	v_fmac_f32_e32 v202, v177, v177
	v_fmac_f32_e32 v202, v178, v178
	v_fmac_f32_e32 v202, v175, v175
	v_fmac_f32_e32 v202, v176, v176
	v_fmac_f32_e32 v202, v173, v173
	v_fmac_f32_e32 v202, v174, v174
	v_fmac_f32_e32 v202, v171, v171
	v_fmac_f32_e32 v202, v172, v172
	v_fmac_f32_e32 v202, v169, v169
	v_fmac_f32_e32 v202, v170, v170
	v_fmac_f32_e32 v202, v167, v167
	v_fmac_f32_e32 v202, v168, v168
	global_load_dwordx4 v[72:75], v213, s[38:39] offset:48
	global_load_dwordx4 v[80:83], v213, s[38:39] offset:32
	global_load_dwordx4 v[84:87], v213, s[38:39] offset:16
	global_load_dwordx4 v[88:91], v213, s[38:39]
	global_load_dwordx4 v[52:55], v213, s[38:39] offset:112
	global_load_dwordx4 v[56:59], v213, s[38:39] offset:96
	global_load_dwordx4 v[60:63], v213, s[38:39] offset:80
	global_load_dwordx4 v[68:71], v213, s[38:39] offset:64
	global_load_dwordx4 v[44:47], v213, s[38:39] offset:512
	global_load_dwordx4 v[40:43], v213, s[38:39] offset:528
	global_load_dwordx4 v[48:51], v213, s[38:39] offset:576
	global_load_dwordx4 v[192:195], v213, s[38:39] offset:592
	v_fmac_f32_e32 v202, v165, v165
	v_fmac_f32_e32 v202, v166, v166
	v_fmac_f32_e32 v202, v164, v164
	v_fmac_f32_e32 v202, v163, v163
	v_fmac_f32_e32 v202, v161, v161
	v_fmac_f32_e32 v202, v160, v160
	v_fmac_f32_e32 v202, v159, v159
	v_fmac_f32_e32 v202, v158, v158
	v_fmac_f32_e32 v202, v157, v157
	v_fmac_f32_e32 v202, v156, v156
	v_fmac_f32_e32 v202, v155, v155
	v_fmac_f32_e32 v202, v154, v154
	v_fmac_f32_e32 v202, v153, v153
	v_fmac_f32_e32 v202, v152, v152
	s_waitcnt vmcnt(25)
	v_lshlrev_b32_e32 v150, 16, v22
	v_fmac_f32_e32 v202, v151, v151
	v_and_b32_e32 v149, 0xffff0000, v22
	v_fmac_f32_e32 v202, v150, v150
	v_lshlrev_b32_e32 v148, 16, v23
	v_fmac_f32_e32 v202, v149, v149
	v_and_b32_e32 v147, 0xffff0000, v23
	v_fmac_f32_e32 v202, v148, v148
	v_lshlrev_b32_e32 v146, 16, v24
	v_fmac_f32_e32 v202, v147, v147
	v_and_b32_e32 v145, 0xffff0000, v24
	v_fmac_f32_e32 v202, v146, v146
	v_lshlrev_b32_e32 v144, 16, v25
	v_fmac_f32_e32 v202, v145, v145
	v_and_b32_e32 v143, 0xffff0000, v25
	v_fmac_f32_e32 v202, v144, v144
	s_waitcnt vmcnt(24)
	v_lshlrev_b32_e32 v142, 16, v26
	v_fmac_f32_e32 v202, v143, v143
	v_and_b32_e32 v141, 0xffff0000, v26
	v_fmac_f32_e32 v202, v142, v142
	v_lshlrev_b32_e32 v140, 16, v27
	v_fmac_f32_e32 v202, v141, v141
	v_and_b32_e32 v139, 0xffff0000, v27
	v_fmac_f32_e32 v202, v140, v140
	v_lshlrev_b32_e32 v138, 16, v28
	v_fmac_f32_e32 v202, v139, v139
	v_and_b32_e32 v137, 0xffff0000, v28
	v_fmac_f32_e32 v202, v138, v138
	v_lshlrev_b32_e32 v136, 16, v29
	v_fmac_f32_e32 v202, v137, v137
	v_and_b32_e32 v135, 0xffff0000, v29
	v_fmac_f32_e32 v202, v136, v136
	s_waitcnt vmcnt(23)
	v_lshlrev_b32_e32 v134, 16, v30
	v_fmac_f32_e32 v202, v135, v135
	v_and_b32_e32 v133, 0xffff0000, v30
	v_fmac_f32_e32 v202, v134, v134
	v_lshlrev_b32_e32 v132, 16, v31
	v_fmac_f32_e32 v202, v133, v133
	v_and_b32_e32 v131, 0xffff0000, v31
	v_fmac_f32_e32 v202, v132, v132
	v_lshlrev_b32_e32 v129, 16, v32
	v_fmac_f32_e32 v202, v131, v131
	v_and_b32_e32 v128, 0xffff0000, v32
	v_fmac_f32_e32 v202, v129, v129
	v_lshlrev_b32_e32 v127, 16, v33
	v_fmac_f32_e32 v202, v128, v128
	v_and_b32_e32 v126, 0xffff0000, v33
	v_fmac_f32_e32 v202, v127, v127
	s_waitcnt vmcnt(22)
	v_lshlrev_b32_e32 v191, 16, v34
	v_fmac_f32_e32 v202, v126, v126
	v_and_b32_e32 v190, 0xffff0000, v34
	v_fmac_f32_e32 v202, v191, v191
	v_lshlrev_b32_e32 v189, 16, v35
	v_fmac_f32_e32 v202, v190, v190
	v_and_b32_e32 v188, 0xffff0000, v35
	v_fmac_f32_e32 v202, v189, v189
	v_lshlrev_b32_e32 v187, 16, v36
	v_fmac_f32_e32 v202, v188, v188
	v_and_b32_e32 v186, 0xffff0000, v36
	v_fmac_f32_e32 v202, v187, v187
	v_lshlrev_b32_e32 v185, 16, v37
	v_fmac_f32_e32 v202, v186, v186
	v_and_b32_e32 v184, 0xffff0000, v37
	v_fmac_f32_e32 v202, v185, v185
	s_waitcnt vmcnt(17)
	v_lshlrev_b32_e32 v125, 16, v76
	v_lshlrev_b32_e32 v124, 16, v64
	v_fmac_f32_e32 v202, v184, v184
	s_waitcnt vmcnt(16)
	v_lshlrev_b32_e32 v31, 16, v119
	v_lshlrev_b32_e32 v30, 16, v115
	s_waitcnt vmcnt(13)
	v_mov_b32_e32 v93, v16
	v_and_b32_e32 v95, 0xffff0000, v119
	v_and_b32_e32 v94, 0xffff0000, v115
	v_mov_b32_e32 v16, v105
	v_lshlrev_b32_e32 v97, 16, v118
	v_lshlrev_b32_e32 v96, 16, v114
	v_mov_b32_e32 v98, v102
	v_mov_b32_e32 v99, v14
	v_and_b32_e32 v101, 0xffff0000, v118
	v_and_b32_e32 v100, 0xffff0000, v114
	v_mov_b32_e32 v14, v103
	v_lshlrev_b32_e32 v103, 16, v117
	v_lshlrev_b32_e32 v102, 16, v113
	s_waitcnt vmcnt(12)
	v_mov_b32_e32 v105, v20
	v_and_b32_e32 v107, 0xffff0000, v117
	v_and_b32_e32 v106, 0xffff0000, v113
	v_mov_b32_e32 v20, v123
	v_lshlrev_b32_e32 v109, 16, v116
	v_mov_b32_e32 v111, v18
	v_and_b32_e32 v113, 0xffff0000, v116
	v_mov_b32_e32 v18, v121
	v_lshlrev_b32_e32 v115, 16, v79
	v_lshlrev_b32_e32 v114, 16, v67
	v_and_b32_e32 v117, 0xffff0000, v79
	v_and_b32_e32 v116, 0xffff0000, v67
	v_lshlrev_b32_e32 v119, 16, v78
	v_lshlrev_b32_e32 v118, 16, v66
	v_and_b32_e32 v79, 0xffff0000, v78
	v_and_b32_e32 v78, 0xffff0000, v66
	v_lshlrev_b32_e32 v121, 16, v77
	v_and_b32_e32 v123, 0xffff0000, v77
	v_and_b32_e32 v77, 0xffff0000, v76
	v_pk_mul_f32 v[66:67], v[124:125], v[124:125]
	v_and_b32_e32 v76, 0xffff0000, v64
	v_mov_b32_e32 v92, v104
	v_mov_b32_e32 v104, v122
	v_mov_b32_e32 v110, v120
	v_lshlrev_b32_e32 v120, 16, v65
	v_and_b32_e32 v122, 0xffff0000, v65
	v_add_f32_e32 v65, v67, v202
	v_pk_mul_f32 v[202:203], v[76:77], v[76:77]
	v_pk_mul_f32 v[198:199], v[120:121], v[120:121]
	v_add_f32_e32 v64, v203, v65
	v_pk_mul_f32 v[200:201], v[122:123], v[122:123]
	v_add_f32_e32 v64, v199, v64
	v_pk_mul_f32 v[196:197], v[118:119], v[118:119]
	v_add_f32_e32 v64, v201, v64
	v_pk_mul_f32 v[220:221], v[78:79], v[78:79]
	v_add_f32_e32 v64, v197, v64
	v_pk_mul_f32 v[216:217], v[114:115], v[114:115]
	v_add_f32_e32 v64, v221, v64
	v_lshlrev_b32_e32 v108, 16, v112
	v_pk_mul_f32 v[218:219], v[116:117], v[116:117]
	v_add_f32_e32 v64, v217, v64
	v_pk_mul_f32 v[214:215], v[108:109], v[108:109]
	v_and_b32_e32 v112, 0xffff0000, v112
	v_add_f32_e32 v64, v219, v64
	v_pk_mul_f32 v[228:229], v[112:113], v[112:113]
	v_add_f32_e32 v64, v215, v64
	v_pk_mul_f32 v[224:225], v[102:103], v[102:103]
	v_add_f32_e32 v64, v229, v64
	v_pk_mul_f32 v[226:227], v[106:107], v[106:107]
	v_add_f32_e32 v64, v225, v64
	v_pk_mul_f32 v[222:223], v[96:97], v[96:97]
	v_add_f32_e32 v64, v227, v64
	v_pk_mul_f32 v[232:233], v[100:101], v[100:101]
	v_add_f32_e32 v64, v223, v64
	v_pk_mul_f32 v[208:209], v[30:31], v[30:31]
	v_add_f32_e32 v64, v233, v64
	v_pk_mul_f32 v[230:231], v[94:95], v[94:95]
	v_add_f32_e32 v64, v209, v64
	v_add_f32_e32 v64, v231, v64
	v_add_f32_e32 v197, v66, v64
	v_add_f32_e32 v197, v202, v197
	v_add_f32_e32 v197, v198, v197
	v_mov_b32_e32 v2, v4
	v_mov_b32_e32 v3, v10
	v_mov_b32_e32 v10, v5
	v_mov_b32_e32 v4, v6
	v_mov_b32_e32 v5, v12
	v_mov_b32_e32 v12, v7
	v_add_f32_e32 v197, v200, v197
	v_pk_add_f32 v[2:3], v[2:3], v[10:11]
	v_pk_add_f32 v[4:5], v[4:5], v[12:13]
	v_add_f32_e32 v209, v196, v197
	v_pk_add_f32 v[2:3], v[2:3], v[4:5]
	v_add_f32_e32 v209, v220, v209
	v_add_f32_e32 v2, v2, v3
	v_add_f32_e32 v209, v216, v209
	v_fmamk_f32 v2, v2, 0x3b000000, v1
	v_add_f32_e32 v209, v218, v209
	v_rsq_f32_e32 v234, v2
	v_and_b32_e32 v2, 63, v9
	v_bfe_u32 v3, v9, 6, 8
	v_add_f32_e32 v209, v214, v209
	v_cndmask_b32_e32 v2, v2, v3, vcc
	v_add_f32_e32 v209, v228, v209
	v_lshlrev_b32_e32 v236, 6, v2
	v_add_f32_e32 v209, v224, v209
	global_load_dwordx4 v[36:39], v236, s[40:41]
	global_load_dwordx4 v[22:25], v236, s[40:41] offset:16
	global_load_dwordx4 v[6:9], v236, s[40:41] offset:32
	global_load_dwordx4 v[2:5], v236, s[40:41] offset:48
	global_load_dwordx4 v[26:29], v236, s[44:45] offset:16
	global_load_dwordx4 v[10:13], v236, s[44:45] offset:32
	global_load_dwordx4 v[32:35], v236, s[44:45] offset:48
	global_load_dwordx4 v[64:67], v236, s[44:45]
	global_load_dwordx4 v[196:199], v213, s[38:39] offset:304
	global_load_dwordx4 v[200:203], v213, s[38:39] offset:288
	global_load_dwordx4 v[214:217], v213, s[38:39] offset:272
	global_load_dwordx4 v[218:221], v213, s[38:39] offset:256
	v_add_f32_e32 v209, v226, v209
	v_add_f32_e32 v209, v222, v209
	v_add_f32_e32 v209, v232, v209
	v_add_f32_e32 v208, v208, v209
	v_add_f32_e32 v230, v230, v208
	s_waitcnt vmcnt(12)
	v_mov_b32_e32 v208, v194
	v_mov_b32_e32 v194, v230
	s_nop 1
	v_permlane32_swap_b32_e32 v230, v194
	v_mul_f32_e32 v235, v234, v234
	v_add_f32_e32 v194, v230, v194
	v_mul_f32_e32 v194, v194, v235
	v_fmamk_f32 v194, v194, 0x3baaaaab, v1
	v_rsq_f32_e32 v230, v194
	v_mov_b32_e32 v194, v192
	global_load_dwordx4 v[222:225], v213, s[38:39] offset:368
	global_load_dwordx4 v[226:229], v213, s[38:39] offset:352
	v_mov_b32_e32 v209, v42
	v_mul_f32_e32 v192, v234, v230
	v_mul_f32_e32 v192, 0x3ea53555, v192
	v_mul_f32_e32 v231, v80, v192
	v_mul_f32_e32 v232, v81, v192
	v_mul_f32_e32 v233, v82, v192
	v_mul_f32_e32 v234, v83, v192
	v_mul_f32_e32 v235, v72, v192
	v_mul_f32_e32 v236, v73, v192
	v_mul_f32_e32 v237, v74, v192
	v_mul_f32_e32 v238, v75, v192
	global_load_dwordx4 v[72:75], v213, s[38:39] offset:336
	global_load_dwordx4 v[80:83], v213, s[38:39] offset:320
	v_mov_b32_e32 v42, v195
	v_mov_b32_e32 v195, v40
	v_mov_b32_e32 v40, v193
	v_mul_f32_e32 v193, v85, v192
	v_mul_f32_e32 v177, v193, v177
	v_mul_f32_e32 v193, v232, v173
	v_mov_b32_e32 v173, v46
	v_mov_b32_e32 v46, v51
	v_mov_b32_e32 v51, v44
	v_mul_f32_e32 v44, v60, v192
	v_mul_f32_e32 v163, v44, v163
	v_mul_f32_e32 v44, v61, v192
	v_mul_f32_e32 v161, v44, v161
	v_mul_f32_e32 v44, v62, v192
	v_mul_f32_e32 v160, v44, v160
	v_mul_f32_e32 v44, v63, v192
	v_mul_f32_e32 v159, v44, v159
	v_mul_f32_e32 v44, v56, v192
	v_mul_f32_e32 v158, v44, v158
	v_mul_f32_e32 v44, v57, v192
	v_mul_f32_e32 v157, v44, v157
	v_mul_f32_e32 v44, v58, v192
	v_mul_f32_e32 v156, v44, v156
	v_mul_f32_e32 v44, v59, v192
	v_mul_f32_e32 v155, v44, v155
	v_mul_f32_e32 v44, v52, v192
	v_mul_f32_e32 v154, v44, v154
	v_mul_f32_e32 v44, v53, v192
	v_mul_f32_e32 v153, v44, v153
	v_mul_f32_e32 v44, v54, v192
	v_mul_f32_e32 v152, v44, v152
	v_mul_f32_e32 v44, v55, v192
	v_mul_f32_e32 v151, v44, v151
	v_pk_mul_f32 v[40:41], v[192:193], v[40:41] op_sel_hi:[0,1]
	v_pk_mul_f32 v[54:55], v[40:41], v[78:79]
	v_pk_mul_f32 v[40:41], v[192:193], v[208:209] op_sel_hi:[0,1]
	v_pk_mul_f32 v[56:57], v[40:41], v[114:115]
	v_pk_mul_f32 v[40:41], v[192:193], v[42:43] op_sel_hi:[0,1]
	v_pk_mul_f32 v[42:43], v[40:41], v[116:117]
	v_pk_mul_f32 v[40:41], v[192:193], v[110:111] op_sel_hi:[0,1]
	v_pk_mul_f32 v[58:59], v[40:41], v[108:109]
	v_pk_mul_f32 v[40:41], v[192:193], v[104:105] op_sel_hi:[0,1]
	v_mul_f32_e32 v176, v231, v176
	v_mul_f32_e32 v231, v235, v172
	v_mov_b32_e32 v172, v50
	v_mov_b32_e32 v50, v48
	v_pk_mul_f32 v[60:61], v[40:41], v[102:103]
	v_pk_mul_f32 v[40:41], v[192:193], v[98:99] op_sel_hi:[0,1]
	v_pk_mul_f32 v[50:51], v[192:193], v[50:51] op_sel_hi:[0,1]
	v_pk_mul_f32 v[62:63], v[40:41], v[96:97]
	v_pk_mul_f32 v[40:41], v[192:193], v[92:93] op_sel_hi:[0,1]
	s_waitcnt vmcnt(4)
	v_mul_f32_e32 v44, v218, v192
	v_mul_f32_e32 v150, v44, v150
	v_mul_f32_e32 v44, v219, v192
	v_mul_f32_e32 v149, v44, v149
	v_mul_f32_e32 v44, v220, v192
	v_mul_f32_e32 v148, v44, v148
	v_mul_f32_e32 v44, v221, v192
	v_mul_f32_e32 v147, v44, v147
	v_mul_f32_e32 v44, v214, v192
	v_mul_f32_e32 v146, v44, v146
	v_mul_f32_e32 v44, v215, v192
	v_mul_f32_e32 v145, v44, v145
	v_mul_f32_e32 v44, v216, v192
	v_mul_f32_e32 v144, v44, v144
	v_mul_f32_e32 v44, v217, v192
	v_mul_f32_e32 v143, v44, v143
	v_mul_f32_e32 v44, v200, v192
	v_mul_f32_e32 v142, v44, v142
	v_mul_f32_e32 v44, v201, v192
	v_mul_f32_e32 v141, v44, v141
	v_mul_f32_e32 v44, v202, v192
	v_mul_f32_e32 v140, v44, v140
	v_mul_f32_e32 v44, v203, v192
	v_mul_f32_e32 v139, v44, v139
	v_mul_f32_e32 v44, v196, v192
	v_mul_f32_e32 v138, v44, v138
	v_mul_f32_e32 v44, v197, v192
	v_mul_f32_e32 v137, v44, v137
	v_mul_f32_e32 v44, v198, v192
	v_mul_f32_e32 v136, v44, v136
	v_mul_f32_e32 v44, v199, v192
	v_mul_f32_e32 v135, v44, v135
	s_waitcnt vmcnt(0)
	v_mul_f32_e32 v44, v192, v80
	v_mul_f32_e32 v80, v44, v134
	v_mul_f32_e32 v44, v192, v81
	v_mul_f32_e32 v81, v44, v133
	v_mul_f32_e32 v44, v192, v82
	v_mul_f32_e32 v82, v44, v132
	v_mul_f32_e32 v44, v192, v83
	v_mul_f32_e32 v83, v44, v131
	v_mul_f32_e32 v44, v192, v72
	v_mul_f32_e32 v72, v44, v129
	v_mul_f32_e32 v44, v192, v73
	v_mul_f32_e32 v73, v44, v128
	v_mul_f32_e32 v44, v192, v74
	v_mul_f32_e32 v74, v44, v127
	v_mul_f32_e32 v44, v192, v75
	v_mul_f32_e32 v75, v44, v126
	v_mul_f32_e32 v44, v192, v226
	v_mul_f32_e32 v126, v44, v191
	v_mul_f32_e32 v44, v192, v227
	v_mul_f32_e32 v127, v44, v190
	v_mul_f32_e32 v44, v192, v228
	v_mul_f32_e32 v128, v44, v189
	v_mul_f32_e32 v44, v192, v229
	v_mul_f32_e32 v129, v44, v188
	v_mul_f32_e32 v44, v192, v222
	v_mul_f32_e32 v131, v44, v187
	v_mul_f32_e32 v44, v192, v223
	v_mul_f32_e32 v132, v44, v186
	v_mul_f32_e32 v44, v192, v224
	v_mul_f32_e32 v133, v44, v185
	v_mul_f32_e32 v44, v192, v225
	v_pk_mul_f32 v[16:17], v[192:193], v[16:17] op_sel_hi:[0,1]
	v_mul_f32_e32 v230, v87, v192
	v_mul_f32_e32 v241, v70, v192
	v_mul_f32_e32 v134, v44, v184
	v_pk_mul_f32 v[50:51], v[50:51], v[124:125]
	v_mov_b32_e32 v44, v49
	v_pk_mul_f32 v[30:31], v[40:41], v[30:31]
	v_pk_mul_f32 v[40:41], v[16:17], v[94:95]
	v_mov_b32_e32 v16, v64
	v_mov_b32_e32 v17, v36
	v_mul_f32_e32 v175, v230, v175
	v_mul_f32_e32 v174, v233, v174
	v_mul_f32_e32 v230, v234, v171
	v_mul_f32_e32 v233, v238, v167
	v_mul_f32_e32 v234, v241, v166
	v_mov_b32_e32 v166, v36
	v_mov_b32_e32 v167, v64
	v_pk_mul_f32 v[44:45], v[192:193], v[44:45] op_sel_hi:[0,1]
	v_pk_mul_f32 v[16:17], v[50:51], v[16:17]
	v_pk_mul_f32 v[44:45], v[44:45], v[76:77]
	v_sub_f32_e32 v76, v17, v16
	v_pk_mul_f32 v[16:17], v[50:51], v[166:167]
	v_mov_b32_e32 v36, v65
	v_add_f32_e32 v50, v16, v17
	v_pk_mul_f32 v[16:17], v[44:45], v[36:37]
	v_mov_b32_e32 v64, v37
	v_pk_mul_f32 v[48:49], v[192:193], v[172:173] op_sel_hi:[0,1]
	v_sub_f32_e32 v36, v17, v16
	v_pk_mul_f32 v[16:17], v[44:45], v[64:65]
	v_pk_mul_f32 v[48:49], v[48:49], v[120:121]
	v_add_f32_e32 v51, v16, v17
	v_mov_b32_e32 v16, v66
	v_mov_b32_e32 v17, v38
	v_mul_f32_e32 v232, v237, v170
	v_mov_b32_e32 v170, v38
	v_mov_b32_e32 v171, v66
	v_pk_mul_f32 v[46:47], v[192:193], v[46:47] op_sel_hi:[0,1]
	v_pk_mul_f32 v[16:17], v[48:49], v[16:17]
	v_pk_mul_f32 v[46:47], v[46:47], v[122:123]
	v_sub_f32_e32 v64, v17, v16
	v_pk_mul_f32 v[16:17], v[48:49], v[170:171]
	v_mov_b32_e32 v38, v67
	v_add_f32_e32 v65, v16, v17
	v_pk_mul_f32 v[16:17], v[46:47], v[38:39]
	v_mov_b32_e32 v66, v39
	v_pk_mul_f32 v[52:53], v[192:193], v[194:195] op_sel_hi:[0,1]
	v_sub_f32_e32 v77, v17, v16
	v_pk_mul_f32 v[16:17], v[46:47], v[66:67]
	v_mul_f32_e32 v90, v90, v192
	v_mul_f32_e32 v91, v91, v192
	v_pk_mul_f32 v[52:53], v[52:53], v[118:119]
	v_add_f32_e32 v66, v16, v17
	v_mov_b32_e32 v16, v26
	v_mov_b32_e32 v17, v22
	v_mul_f32_e32 v213, v90, v182
	v_mul_f32_e32 v179, v91, v179
	v_mov_b32_e32 v90, v22
	v_mov_b32_e32 v91, v26
	v_pk_mul_f32 v[16:17], v[52:53], v[16:17]
	v_mov_b32_e32 v22, v27
	v_sub_f32_e32 v37, v17, v16
	v_pk_mul_f32 v[16:17], v[52:53], v[90:91]
	v_mov_b32_e32 v26, v23
	v_add_f32_e32 v52, v16, v17
	v_pk_mul_f32 v[16:17], v[54:55], v[22:23]
	v_mul_f32_e32 v88, v88, v192
	v_sub_f32_e32 v38, v17, v16
	v_pk_mul_f32 v[16:17], v[54:55], v[26:27]
	v_mul_f32_e32 v89, v89, v192
	v_add_f32_e32 v53, v16, v17
	v_mov_b32_e32 v16, v28
	v_mov_b32_e32 v17, v24
	v_mul_f32_e32 v183, v88, v183
	v_mul_f32_e32 v181, v89, v181
	v_mov_b32_e32 v88, v24
	v_mov_b32_e32 v89, v28
	v_pk_mul_f32 v[16:17], v[56:57], v[16:17]
	v_mov_b32_e32 v24, v29
	v_sub_f32_e32 v54, v17, v16
	v_pk_mul_f32 v[16:17], v[56:57], v[88:89]
	v_mov_b32_e32 v28, v25
	v_add_f32_e32 v55, v16, v17
	v_pk_mul_f32 v[16:17], v[42:43], v[24:25]
	v_mul_f32_e32 v86, v86, v192
	v_sub_f32_e32 v56, v17, v16
	v_pk_mul_f32 v[16:17], v[42:43], v[28:29]
	v_mul_f32_e32 v178, v86, v178
	v_add_f32_e32 v57, v16, v17
	v_mov_b32_e32 v16, v10
	v_mov_b32_e32 v17, v6
	v_mov_b32_e32 v86, v6
	v_mov_b32_e32 v87, v10
	v_pk_mul_f32 v[18:19], v[192:193], v[18:19] op_sel_hi:[0,1]
	v_pk_mul_f32 v[16:17], v[58:59], v[16:17]
	v_pk_mul_f32 v[18:19], v[18:19], v[112:113]
	v_sub_f32_e32 v39, v17, v16
	v_pk_mul_f32 v[16:17], v[58:59], v[86:87]
	v_mov_b32_e32 v6, v11
	v_mov_b32_e32 v10, v7
	v_mul_f32_e32 v84, v84, v192
	v_add_f32_e32 v58, v16, v17
	v_pk_mul_f32 v[16:17], v[18:19], v[6:7]
	v_pk_mul_f32 v[6:7], v[18:19], v[10:11]
	v_mul_f32_e32 v239, v68, v192
	v_mul_f32_e32 v240, v69, v192
	v_mul_f32_e32 v182, v84, v180
	v_add_f32_e32 v67, v6, v7
	v_mov_b32_e32 v6, v12
	v_mov_b32_e32 v7, v8
	v_mov_b32_e32 v180, v205
	v_mul_f32_e32 v242, v71, v192
	v_mov_b32_e32 v84, v8
	v_mov_b32_e32 v85, v12
	v_mul_f32_e32 v169, v236, v169
	v_mul_f32_e32 v168, v239, v168
	v_mul_f32_e32 v165, v240, v165
	v_pk_mul_f32 v[20:21], v[192:193], v[20:21] op_sel_hi:[0,1]
	v_pk_mul_f32 v[6:7], v[60:61], v[6:7]
	v_cvt_pk_fp8_f32 v180, v183, v181
	v_mov_b32_e32 v183, v205
	v_mov_b32_e32 v184, v205
	v_mul_f32_e32 v235, v242, v164
	v_pk_mul_f32 v[20:21], v[20:21], v[106:107]
	v_sub_f32_e32 v78, v7, v6
	v_pk_mul_f32 v[6:7], v[60:61], v[84:85]
	v_mov_b32_e32 v8, v13
	v_cvt_pk_fp8_f32 v183, v231, v169
	v_cvt_pk_fp8_f32 v184, v168, v165
	v_mov_b32_e32 v185, v205
	v_mov_b32_e32 v164, v162
	v_mov_b32_e32 v165, v162
	v_mov_b32_e32 v166, v162
	v_mov_b32_e32 v167, v162
	v_mov_b32_e32 v168, v162
	v_mov_b32_e32 v169, v162
	v_add_f32_e32 v60, v6, v7
	v_pk_mul_f32 v[6:7], v[20:21], v[8:9]
	v_mov_b32_e32 v12, v9
	v_cvt_pk_fp8_f32 v185, v163, v161
	v_mov_b32_e32 v163, v162
	v_mov_b64_e32 v[170:171], v[168:169]
	v_sub_f32_e32 v61, v7, v6
	v_pk_mul_f32 v[6:7], v[20:21], v[12:13]
	v_mov_b32_e32 v181, v205
	v_mov_b64_e32 v[168:169], v[166:167]
	v_mov_b64_e32 v[166:167], v[164:165]
	v_mov_b64_e32 v[164:165], v[162:163]
	s_cselect_b32 s7, s10, s12
	s_cselect_b32 s6, s9, s11
	s_add_i32 s13, s65, 0xb800
	v_add_f32_e32 v79, v6, v7
	v_mov_b32_e32 v6, v32
	v_mov_b32_e32 v7, v2
	v_cvt_pk_fp8_f32 v181, v182, v177
	v_mov_b32_e32 v182, v205
	v_mov_b32_e32 v186, v205
	v_mov_b32_e32 v187, v205
	s_mov_b32 s14, m0
	s_mov_b32 m0, s13
	s_nop 0
	global_load_lds_dwordx4 v211, s[6:7]
	s_mov_b32 m0, s14
	s_and_b64 s[6:7], exec, s[54:55]
	v_mov_b32_e32 v70, v2
	v_mov_b32_e32 v71, v32
	v_pk_mul_f32 v[14:15], v[192:193], v[14:15] op_sel_hi:[0,1]
	v_pk_mul_f32 v[6:7], v[62:63], v[6:7]
	v_cvt_pk_fp8_f32 v182, v176, v193
	v_cvt_pk_fp8_f32 v186, v158, v157
	s_cselect_b32 s7, s10, s12
	s_cselect_b32 s6, s9, s11
	s_add_i32 s9, s64, 0xb800
	s_mov_b32 s10, m0
	s_mov_b32 m0, s9
	s_nop 0
	global_load_lds_dwordx4 v210, s[6:7]
	s_mov_b32 m0, s10
	v_cvt_pk_fp8_f32 v187, v154, v153
	v_pk_mul_f32 v[14:15], v[14:15], v[100:101]
	v_sub_f32_e32 v84, v7, v6
	v_pk_mul_f32 v[6:7], v[62:63], v[70:71]
	v_mov_b32_e32 v2, v33
	s_add_i32 s9, s33, 0xb800
	s_mov_b32 s10, m0
	s_mov_b32 m0, s9
	s_nop 0
	global_load_lds_dwordx4 v212, s[6:7]
	s_mov_b32 m0, s10
	v_add_f32_e32 v62, v6, v7
	v_pk_mul_f32 v[6:7], v[14:15], v[2:3]
	v_mov_b32_e32 v32, v3
	v_cvt_pk_fp8_f32 v180, v213, v179 op_sel:[0,0,1]
	s_waitcnt vmcnt(0) lgkmcnt(0)
	s_barrier
	v_add_u32_e32 v213, 0, v204
	v_sub_f32_e32 v63, v7, v6
	v_pk_mul_f32 v[2:3], v[14:15], v[32:33]
	ds_read_b128 v[6:9], v213
	ds_read_b128 v[10:13], v213 offset:16
	v_add_f32_e32 v70, v2, v3
	v_mov_b32_e32 v2, v34
	v_mov_b32_e32 v3, v4
	v_cvt_pk_fp8_f32 v181, v178, v175 op_sel:[0,0,1]
	v_cvt_pk_fp8_f32 v182, v174, v230 op_sel:[0,0,1]
	v_cvt_pk_fp8_f32 v183, v232, v233 op_sel:[0,0,1]
	v_cvt_pk_fp8_f32 v184, v234, v235 op_sel:[0,0,1]
	v_cvt_pk_fp8_f32 v185, v160, v159 op_sel:[0,0,1]
	v_cvt_pk_fp8_f32 v186, v156, v155 op_sel:[0,0,1]
	v_cvt_pk_fp8_f32 v187, v152, v151 op_sel:[0,0,1]
	v_mov_b32_e32 v68, v4
	v_mov_b32_e32 v69, v34
	v_pk_mul_f32 v[2:3], v[30:31], v[2:3]
	v_mov_b32_e32 v4, v35
	v_sub_f32_e32 v71, v3, v2
	v_pk_mul_f32 v[2:3], v[30:31], v[68:69]
	v_mov_b32_e32 v34, v5
	v_add_f32_e32 v68, v2, v3
	v_pk_mul_f32 v[2:3], v[40:41], v[4:5]
	s_waitcnt lgkmcnt(0)
	v_mfma_f32_32x32x64_f8f6f4 v[18:33], v[6:13], v[180:187], 0
	v_sub_f32_e32 v69, v3, v2
	ds_read_b128 v[2:5], v213 offset:6656
	ds_read_b128 v[6:9], v213 offset:6672
	v_sub_f32_e32 v59, v17, v16
	v_mov_b32_e32 v188, v205
	v_mov_b32_e32 v189, v205
	v_mov_b32_e32 v190, v205
	v_mov_b32_e32 v191, v205
	v_mov_b32_e32 v192, v205
	v_mov_b32_e32 v193, v205
	v_mov_b32_e32 v194, v205
	v_mov_b32_e32 v195, v205
	v_cvt_pk_fp8_f32 v188, v150, v149
	v_cvt_pk_fp8_f32 v189, v146, v145
	v_cvt_pk_fp8_f32 v190, v142, v141
	v_cvt_pk_fp8_f32 v191, v138, v137
	s_waitcnt lgkmcnt(0)
	v_mfma_f32_32x32x64_f8f6f4 v[2:17], v[2:9], v[180:187], 0
	v_cvt_pk_fp8_f32 v192, v80, v81
	v_cvt_pk_fp8_f32 v193, v72, v73
	v_cvt_pk_fp8_f32 v194, v126, v127
	v_cvt_pk_fp8_f32 v195, v131, v132
	ds_read_b128 v[42:45], v213 offset:64
	ds_read_b128 v[46:49], v213 offset:80
	v_cvt_pk_fp8_f32 v188, v148, v147 op_sel:[0,0,1]
	v_cvt_pk_fp8_f32 v189, v144, v143 op_sel:[0,0,1]
	v_cvt_pk_fp8_f32 v190, v140, v139 op_sel:[0,0,1]
	v_cvt_pk_fp8_f32 v191, v136, v135 op_sel:[0,0,1]
	v_cvt_pk_fp8_f32 v192, v82, v83 op_sel:[0,0,1]
	v_cvt_pk_fp8_f32 v193, v74, v75 op_sel:[0,0,1]
	v_cvt_pk_fp8_f32 v194, v128, v129 op_sel:[0,0,1]
	v_cvt_pk_fp8_f32 v195, v133, v134 op_sel:[0,0,1]
	v_pk_mul_f32 v[34:35], v[40:41], v[34:35]
	v_mov_b32_e32 v196, v205
	v_mov_b32_e32 v197, v205
	v_mov_b32_e32 v198, v205
	v_add_f32_e32 v72, v34, v35
	s_waitcnt lgkmcnt(0)
	v_mfma_f32_32x32x64_f8f6f4 v[18:33], v[42:49], v[188:195], v[18:33]
	v_cvt_pk_fp8_f32 v196, v76, v36
	v_cvt_pk_fp8_f32 v197, v37, v38
	v_cvt_pk_fp8_f32 v198, v39, v59
	ds_read_b128 v[34:37], v213 offset:6720
	ds_read_b128 v[38:41], v213 offset:6736
	v_mov_b32_e32 v199, v205
	v_mov_b32_e32 v200, v205
	v_mov_b32_e32 v201, v205
	v_mov_b32_e32 v202, v205
	v_mov_b32_e32 v203, v205
	v_cvt_pk_fp8_f32 v199, v84, v63
	v_cvt_pk_fp8_f32 v200, v50, v51
	v_cvt_pk_fp8_f32 v201, v52, v53
	v_cvt_pk_fp8_f32 v202, v58, v67
	v_cvt_pk_fp8_f32 v203, v62, v70
	v_cvt_pk_fp8_f32 v196, v64, v77 op_sel:[0,0,1]
	s_waitcnt lgkmcnt(0)
	v_mfma_f32_32x32x64_f8f6f4 v[2:17], v[34:41], v[188:195], v[2:17]
	ds_read_b128 v[34:37], v213 offset:128
	ds_read_b128 v[38:41], v213 offset:144
	v_cvt_pk_fp8_f32 v197, v54, v56 op_sel:[0,0,1]
	v_cvt_pk_fp8_f32 v198, v78, v61 op_sel:[0,0,1]
	v_cvt_pk_fp8_f32 v199, v71, v69 op_sel:[0,0,1]
	v_cvt_pk_fp8_f32 v200, v65, v66 op_sel:[0,0,1]
	v_cvt_pk_fp8_f32 v201, v55, v57 op_sel:[0,0,1]
	v_cvt_pk_fp8_f32 v202, v60, v79 op_sel:[0,0,1]
	v_cvt_pk_fp8_f32 v203, v68, v72 op_sel:[0,0,1]
	s_mov_b32 s9, s8
	s_mov_b32 s10, s8
	s_mov_b32 s11, s8
	s_mov_b32 s12, s8
	s_mov_b32 s13, s8
	s_mov_b32 s14, s8
	v_mov_b64_e32 v[80:81], s[22:23]
	s_waitcnt lgkmcnt(0)
	v_mfma_f32_32x32x64_f8f6f4 v[18:33], v[34:41], v[196:203], v[18:33]
	ds_read_b128 v[34:37], v213 offset:6784
	ds_read_b128 v[38:41], v213 offset:6800
	v_mov_b64_e32 v[78:79], s[20:21]
	v_mov_b64_e32 v[76:77], s[18:19]
	v_mov_b64_e32 v[74:75], s[16:17]
	v_mov_b64_e32 v[72:73], s[14:15]
	v_mov_b64_e32 v[70:71], s[12:13]
	v_mov_b64_e32 v[68:69], s[10:11]
	v_mov_b64_e32 v[66:67], s[8:9]
	s_add_u32 s10, s58, 0x8000
	s_addc_u32 s11, s59, 0
	v_mad_u32_u24 v163, v206, s89, v130
	s_add_u32 s12, s56, 0x200000
	v_mov_b64_e32 v[50:51], v[66:67]
	v_add_u32_e32 v214, 0, v163
	v_lshl_add_u32 v209, v206, 2, s51
	s_waitcnt lgkmcnt(0)
	v_mfma_f32_32x32x64_f8f6f4 v[2:17], v[34:41], v[196:203], v[2:17]
	s_nop 1
	v_max_f32_e32 v34, v19, v19
	v_max_f32_e32 v35, v18, v18
	v_max_f32_e32 v34, v35, v34
	v_lshlrev_b32_e32 v208, 4, v207
	s_addc_u32 s13, s57, 0
	s_mov_b32 s9, 0
	s_mov_b32 s14, -1
	v_mov_b32_e32 v172, 0
	v_mov_b32_e32 v173, 0
	v_mov_b32_e32 v174, 0
	v_mov_b32_e32 v175, 0
	v_mov_b32_e32 v176, 0
	v_mov_b32_e32 v177, 0
	v_mov_b32_e32 v178, 0
	v_mov_b32_e32 v179, 0
	s_nop 2
	v_max3_f32 v35, v20, v21, v3
	v_max3_f32 v34, v34, v2, v4
	v_max3_f32 v34, v34, v5, v22
	v_max3_f32 v35, v35, v24, v25
	v_max3_f32 v34, v34, v23, v6
	v_max3_f32 v35, v35, v8, v9
	v_max3_f32 v34, v34, v7, v26
	v_max3_f32 v35, v35, v28, v29
	v_max3_f32 v34, v34, v27, v10
	v_max3_f32 v35, v35, v12, v13
	v_max3_f32 v34, v34, v11, v30
	v_max3_f32 v35, v35, v32, v33
	v_max3_f32 v34, v34, v31, v14
	v_max3_f32 v35, v35, v16, v17
	v_max3_f32 v34, v34, v15, v35
	v_mov_b32_e32 v35, v34
	s_nop 1
	v_permlane32_swap_b32_e32 v34, v35
	v_max_f32 v34, v34, v35
	v_mov_b64_e32 v[52:53], v[68:69]
	v_add_f32_e32 v34, 0xc0e00000, v34
	v_sub_f32_e32 v82, 0, v34
	v_sub_f32_e32 v113, v33, v34
	v_sub_f32_e32 v112, v32, v34
	v_sub_f32_e32 v111, v31, v34
	v_sub_f32_e32 v110, v30, v34
	v_sub_f32_e32 v109, v29, v34
	v_sub_f32_e32 v108, v28, v34
	v_sub_f32_e32 v107, v27, v34
	v_sub_f32_e32 v106, v26, v34
	v_sub_f32_e32 v105, v25, v34
	v_sub_f32_e32 v104, v24, v34
	v_sub_f32_e32 v103, v23, v34
	v_sub_f32_e32 v102, v22, v34
	v_sub_f32_e32 v101, v21, v34
	v_sub_f32_e32 v100, v20, v34
	v_sub_f32_e32 v99, v19, v34
	v_sub_f32_e32 v98, v18, v34
	v_sub_f32_e32 v129, v17, v34
	v_sub_f32_e32 v128, v16, v34
	v_sub_f32_e32 v127, v15, v34
	v_sub_f32_e32 v126, v14, v34
	v_sub_f32_e32 v125, v13, v34
	v_sub_f32_e32 v124, v12, v34
	v_sub_f32_e32 v123, v11, v34
	v_sub_f32_e32 v122, v10, v34
	v_sub_f32_e32 v121, v9, v34
	v_sub_f32_e32 v120, v8, v34
	v_sub_f32_e32 v119, v7, v34
	v_sub_f32_e32 v118, v6, v34
	v_sub_f32_e32 v117, v5, v34
	v_sub_f32_e32 v116, v4, v34
	v_sub_f32_e32 v115, v3, v34
	v_sub_f32_e32 v114, v2, v34
	v_mov_b64_e32 v[2:3], v[66:67]
	v_mov_b64_e32 v[18:19], v[66:67]
	v_mov_b64_e32 v[34:35], v[66:67]
	v_mov_b32_e32 v83, v82
	v_mov_b32_e32 v84, v82
	v_mov_b32_e32 v85, v82
	v_mov_b32_e32 v86, v82
	v_mov_b32_e32 v87, v82
	v_mov_b32_e32 v88, v82
	v_mov_b32_e32 v89, v82
	v_mov_b32_e32 v90, v82
	v_mov_b32_e32 v91, v82
	v_mov_b32_e32 v92, v82
	v_mov_b32_e32 v93, v82
	v_mov_b32_e32 v94, v82
	v_mov_b32_e32 v95, v82
	v_mov_b32_e32 v96, v82
	v_mov_b32_e32 v97, v82
	v_mov_b64_e32 v[4:5], v[68:69]
	v_mov_b64_e32 v[6:7], v[70:71]
	v_mov_b64_e32 v[8:9], v[72:73]
	v_mov_b64_e32 v[10:11], v[74:75]
	v_mov_b64_e32 v[12:13], v[76:77]
	v_mov_b64_e32 v[14:15], v[78:79]
	v_mov_b64_e32 v[16:17], v[80:81]
	v_mov_b64_e32 v[20:21], v[68:69]
	v_mov_b64_e32 v[22:23], v[70:71]
	v_mov_b64_e32 v[24:25], v[72:73]
	v_mov_b64_e32 v[26:27], v[74:75]
	v_mov_b64_e32 v[28:29], v[76:77]
	v_mov_b64_e32 v[30:31], v[78:79]
	v_mov_b64_e32 v[32:33], v[80:81]
	v_mov_b64_e32 v[36:37], v[68:69]
	v_mov_b64_e32 v[38:39], v[70:71]
	v_mov_b64_e32 v[40:41], v[72:73]
	v_mov_b64_e32 v[42:43], v[74:75]
	v_mov_b64_e32 v[44:45], v[76:77]
	v_mov_b64_e32 v[46:47], v[78:79]
	v_mov_b64_e32 v[48:49], v[80:81]
	v_mov_b64_e32 v[54:55], v[70:71]
	v_mov_b64_e32 v[56:57], v[72:73]
	v_mov_b64_e32 v[58:59], v[74:75]
	v_mov_b64_e32 v[60:61], v[76:77]
	v_mov_b64_e32 v[62:63], v[78:79]
	v_mov_b64_e32 v[64:65], v[80:81]
	s_nop 0
	v_readfirstlane_b32 s100, v0
	s_nop 3
	s_lshr_b32 s100, s100, 8
	s_cmp_eq_u32 s100, 0
	s_cbranch_scc1 .Lmla_prio_lead
	s_setprio 1

.LBB0_567:
	s_nop 0
	s_add_i32 s6, s16, 0x5c00
	s_cmp_lt_i32 s9, 4
	s_cselect_b32 s6, s6, 0
	s_add_i32 s10, s6, 0
	v_add_u32_e32 v213, s10, v204
	ds_read_b128 v[130:133], v213
	ds_read_b128 v[134:137], v213 offset:16
	ds_read_b128 v[214:217], v213 offset:6656
	ds_read_b128 v[218:221], v213 offset:6672
	s_cmp_gt_i32 s9, 1
	s_cselect_b32 s6, -2, 3
	s_add_i32 s6, s6, s9
	s_waitcnt lgkmcnt(2)
	v_mfma_f32_32x32x64_f8f6f4 v[146:161], v[130:137], v[180:187], v[82:97]
	v_exp_f32_e32 v98, v98
	v_exp_f32_e32 v99, v99
	v_exp_f32_e32 v102, v102
	v_exp_f32_e32 v103, v103
	v_exp_f32_e32 v106, v106
	v_exp_f32_e32 v107, v107
	v_exp_f32_e32 v110, v110
	v_exp_f32_e32 v111, v111
	v_exp_f32_e32 v114, v114
	v_exp_f32_e32 v115, v115
	v_exp_f32_e32 v118, v118
	v_exp_f32_e32 v119, v119
	v_exp_f32_e32 v122, v122
	v_exp_f32_e32 v123, v123
	v_exp_f32_e32 v126, v126
	s_waitcnt lgkmcnt(0)
	v_mfma_f32_32x32x64_f8f6f4 v[130:145], v[214:221], v[180:187], v[82:97]
	ds_read_b128 v[214:217], v213 offset:64
	ds_read_b128 v[218:221], v213 offset:80
	v_exp_f32_e32 v127, v127
	s_add_u32 s12, s56, 0x8180000
	s_addc_u32 s13, s57, 0
	s_add_u32 s14, s58, 0x206000
	s_addc_u32 s15, s59, 0
	v_exp_f32_e32 v100, v100
	v_exp_f32_e32 v101, v101
	v_exp_f32_e32 v104, v104
	v_exp_f32_e32 v105, v105
	v_exp_f32_e32 v108, v108
	v_exp_f32_e32 v109, v109
	v_exp_f32_e32 v112, v112
	v_exp_f32_e32 v113, v113
	v_exp_f32_e32 v116, v116
	s_waitcnt lgkmcnt(0)
	v_mfma_f32_32x32x64_f8f6f4 v[146:161], v[214:221], v[188:195], v[146:161]
	ds_read_b128 v[214:217], v213 offset:6720
	ds_read_b128 v[218:221], v213 offset:6736
	v_exp_f32_e32 v117, v117
	v_exp_f32_e32 v120, v120
	v_exp_f32_e32 v121, v121
	v_exp_f32_e32 v124, v124
	v_exp_f32_e32 v125, v125
	v_exp_f32_e32 v128, v128
	v_exp_f32_e32 v129, v129
	v_cvt_pk_fp8_f32 v172, v98, v99
	v_cvt_pk_fp8_f32 v173, v102, v103
	v_cvt_pk_fp8_f32 v174, v106, v107
	v_cvt_pk_fp8_f32 v175, v110, v111
	v_cvt_pk_fp8_f32 v176, v114, v115
	v_cvt_pk_fp8_f32 v177, v118, v119
	v_cvt_pk_fp8_f32 v178, v122, v123
	s_waitcnt lgkmcnt(0)
	v_mfma_f32_32x32x64_f8f6f4 v[130:145], v[214:221], v[188:195], v[130:145]
	v_cvt_pk_fp8_f32 v179, v126, v127
	s_mul_i32 s11, s6, 0x5c00
	s_and_b64 s[6:7], s[52:53], exec
	s_cselect_b32 s7, s13, s15
	s_cselect_b32 s6, s12, s14
	s_add_i32 s17, s11, s65
	ds_read_b128 v[214:217], v213 offset:128
	ds_read_b128 v[218:221], v213 offset:144
	ds_read_b128 v[222:225], v213 offset:6784
	ds_read_b128 v[226:229], v213 offset:6800
	s_mov_b32 s18, m0
	s_mov_b32 m0, s17
	s_nop 0
	global_load_lds_dwordx4 v211, s[6:7]
	s_mov_b32 m0, s18
	s_and_b64 s[6:7], exec, s[54:55]
	s_cselect_b32 s7, s13, s15
	s_cselect_b32 s6, s12, s14
	s_add_i32 s12, s11, s64
	s_mov_b32 s13, m0
	s_mov_b32 m0, s12
	s_nop 0
	global_load_lds_dwordx4 v210, s[6:7]
	s_mov_b32 m0, s13
	v_cvt_pk_fp8_f32 v172, v100, v101 op_sel:[0,0,1]
	v_cvt_pk_fp8_f32 v173, v104, v105 op_sel:[0,0,1]
	v_cvt_pk_fp8_f32 v174, v108, v109 op_sel:[0,0,1]
	v_cvt_pk_fp8_f32 v175, v112, v113 op_sel:[0,0,1]
	v_cvt_pk_fp8_f32 v176, v116, v117 op_sel:[0,0,1]
	v_cvt_pk_fp8_f32 v177, v120, v121 op_sel:[0,0,1]
	v_cvt_pk_fp8_f32 v178, v124, v125 op_sel:[0,0,1]
	v_cvt_pk_fp8_f32 v179, v128, v129 op_sel:[0,0,1]
	s_add_i32 s11, s11, s33
	s_mov_b32 s12, m0
	s_mov_b32 m0, s11
	s_nop 0
	global_load_lds_dwordx4 v212, s[6:7]
	s_mov_b32 m0, s12
	s_add_i32 s6, s16, 0
	v_add_u32_e32 v106, s6, v163
	ds_read_b128 v[98:101], v106 offset:13312
	ds_read_b128 v[102:105], v106 offset:13328
	s_waitcnt lgkmcnt(0)
	v_mfma_f32_32x32x64_f8f6f4 v[50:65], v[172:179], v[98:105], v[50:65]
	ds_read_b128 v[98:101], v106 offset:15872
	ds_read_b128 v[102:105], v106 offset:15888
	v_mfma_f32_32x32x64_f8f6f4 v[146:161], v[214:221], v[196:203], v[146:161]
	v_mfma_f32_32x32x64_f8f6f4 v[130:145], v[222:229], v[196:203], v[130:145]
	s_nop 15
	s_nop 2
	v_max_f32_e32 v107, v146, v146
	s_waitcnt lgkmcnt(0)
	v_mfma_f32_32x32x64_f8f6f4 v[34:49], v[172:179], v[98:105], v[34:49]
	ds_read_b128 v[98:101], v106 offset:18432
	ds_read_b128 v[102:105], v106 offset:18448
	s_waitcnt lgkmcnt(0)
	v_mfma_f32_32x32x64_f8f6f4 v[18:33], v[172:179], v[98:105], v[18:33]
	ds_read_b128 v[98:101], v106 offset:20992
	ds_read_b128 v[102:105], v106 offset:21008
	v_max_f32_e32 v106, v147, v147
	v_max_f32_e32 v106, v107, v106
	v_max3_f32 v107, v148, v149, v131
	v_max3_f32 v106, v106, v130, v132
	v_max3_f32 v106, v106, v133, v150
	v_max3_f32 v107, v107, v152, v153
	v_max3_f32 v106, v106, v151, v134
	s_waitcnt lgkmcnt(0)
	v_mfma_f32_32x32x64_f8f6f4 v[2:17], v[172:179], v[98:105], v[2:17]
	v_max3_f32 v98, v107, v136, v137
	v_max3_f32 v99, v106, v135, v154
	v_max3_f32 v98, v98, v156, v157
	v_max3_f32 v99, v99, v155, v138
	v_max3_f32 v98, v98, v140, v141
	v_max3_f32 v99, v99, v139, v158
	v_max3_f32 v98, v98, v160, v161
	v_max3_f32 v99, v99, v159, v142
	v_max3_f32 v98, v98, v144, v145
	v_max3_f32 v98, v99, v143, v98
	v_mov_b32_e32 v99, v98
	s_nop 1
	v_permlane32_swap_b32_e32 v98, v99
	v_max_f32 v98, v98, v99
	v_mfma_f32_32x32x64_f8f6f4 v[66:81], v[172:179], v[164:171], v[66:81]
	v_cmp_ge_f32_e64 s[6:7], s90, v98
	s_cmp_eq_u64 s[6:7], exec
	s_cbranch_scc0 .LBB0_589
